# speedup vs baseline: 1.0654x; 1.0207x over previous
_ZN2g817gemm_256sq_8phaseEPKDF16_S1_PfPKff:
	s_cmp_ge_u32 s2, 256
	s_cbranch_scc1 .Lg8_nosleep
	s_lshr_b32 s30, s2, 3
	s_and_b32 s30, s30, 3
	s_cmp_eq_u32 s30, 0
	s_cbranch_scc1 .Lg8_nosleep
	s_mul_i32 s30, s30, 1
.Lg8_sleep:
	s_sleep 24
	s_sub_u32 s30, s30, 1
	s_cmp_lg_u32 s30, 0
	s_cbranch_scc1 .Lg8_sleep
.Lg8_nosleep:
	s_ashr_i32 s3, s2, 31
	s_load_dwordx4 s[8:11], s[0:1], 0x0
	s_lshr_b32 s3, s3, 29
	s_add_i32 s6, s2, s3
	s_and_b32 s3, s6, -8
	s_sub_i32 s5, s2, s3
	s_cmp_gt_i32 s5, -1
	s_cbranch_scc0 .LBB1_2
	s_lshl_b32 s4, s5, 7
	s_ashr_i32 s2, s6, 3
	s_cbranch_execz .LBB1_3
	s_branch .LBB1_4
